# seam-wait hosting: during seams 4-7 waves 1-7 of every workgroup convert one w_up tile each while wave 0 runs the grid-barrier protocol; P4 converts 7168 items less
# speedup vs baseline: 1.0051x; 1.0051x over previous
; #define LAS __attribute__((address_space(3)))
; #define LAS __attribute__((address_space(3)))
;     LAS unsigned* scr = (LAS unsigned*)(lds + wave * 16384);
;     WItem d0, d1; WRegs R0, R1;
;     constexpr int KB_ = DM / 32;
;     constexpr int NALL = EARLY ? KB_ * (INW / 128) : KB_ * (DM / 128) + KB_ * (CW / 128) + KB_ * (2 * CW / 128) + (CW / 32) * (DM / 128) + KB_ * (DFF2 / 128) + (DFF / 32) * (DM / 128);
;     const int hi_all = it_hi < NALL ? it_hi : NALL, total = hi_all - it_lo, nwgs = NGW / NWAVES, chunk = (((total + nwgs - 1) / nwgs) + NWAVES - 1) / NWAVES * NWAVES;
;     int it = it_lo + (gw / NWAVES) * chunk + (gw % NWAVES); const int wend0 = it_lo + (gw / NWAVES + 1) * chunk, wend = wend0 < hi_all ? wend0 : hi_all;
; __global__ void __launch_bounds__(NWAVES * 64, 2) mk_fwd(Args args) {
;     ...
;         const int NCONV = (CONV_OVERLAP && G >= 128) ? 51 : 0;
;         if (bx < NCONV) convert_weights<false, true>(P, lds, bx * NWAVES + wave, NCONV * NWAVES, wave, lane, 0, (CONV_OVERLAP && G >= 192) ? LATE_SPLIT : 0x7fffffff);
;         else {
;             sb_phase(lds, PROJ, (bf16*)(ws + WS_MIX), (const float*)(ws + WS_RSB), P.sbo_norm, bx - NCONV, G - NCONV, tid);
;             ret_out_phase(lds, PROJ, (bf16*)(ws + WS_MIX), (const bf16*)(ws + WS_ST), P.ret_norm, bx - NCONV, G - NCONV, tid);
;         }
;         if (NCONV == 0) convert_weights<false>(P, lds, gw, NGW, wave, lane);
.LBB0_519:
	s_mov_b32 s98, 0
	s_mov_b32 s99, 0
	s_mov_b32 s100, s80
	s_mov_b32 s101, s56
	s_mov_b32 s0, 0x9900
	s_cmp_eq_u32 s80, 0x100
	s_cselect_b32 s1, 1, 0
	s_cmp_gt_i32 s75, 6
	s_cselect_b32 s1, s1, 0
	s_cmp_lg_u32 s1, 0
	s_cselect_b32 s0, 0x6000, s0
	s_cmp_eq_u32 s74, 0
	s_cselect_b32 s1, s1, 0
	s_cmp_eq_u32 s75, 12
	s_cselect_b32 s1, s1, 0
	s_cmp_lg_u32 s1, 0
	s_cselect_b32 s0, 0x4400, s0
	v_writelane_b32 v255, s0, 2
	s_mov_b32 s0, 0
	v_writelane_b32 v255, s0, 3

;     ...
;     while (v0) {
;         const bool v1 = it + ST < wend && witem_decode<EARLY>(P, it + ST, d1);
;         if (PIPE) { if (!v1) d1 = d0; witem_load<true>(d1, R1, lane); } else if (v1) witem_load<false>(d1, R1, lane);
;         witem_store(d0, R0, scr, lane);
;         if (!v1) break;
;         v0 = it + 2 * ST < wend && witem_decode<EARLY>(P, it + 2 * ST, d0);
;         if (PIPE) { if (!v0) d0 = d1; witem_load<true>(d0, R0, lane); } else if (v0) witem_load<false>(d0, R0, lane);
;         witem_store(d1, R1, scr, lane);
;         it += 2 * ST;
;     }
; }
; __global__ void __launch_bounds__(NWAVES * 64, 2) mk_fwd(Args args) {
;     ...
;         if (NCONV == 0) convert_weights<false>(P, lds, gw, NGW, wave, lane);
;         __syncthreads();
.LBB0_727:
	s_waitcnt vmcnt(0) lgkmcnt(0)
	s_cmp_ge_u32 s98, 3
	s_cbranch_scc1 .Lsh_dispatch
	s_barrier
	s_cmp_lg_u32 s98, 0
	s_cbranch_scc1 .Lp6_conv_ret
	s_branch .LBB0_728
.Lsh_dispatch:
	s_cmp_eq_u32 s98, 4
	s_cbranch_scc1 .Lsh_ret_4
	s_cmp_eq_u32 s98, 5
	s_cbranch_scc1 .Lsh_ret_5
	s_cmp_eq_u32 s98, 6
	s_cbranch_scc1 .Lsh_ret_6
	s_branch .Lsh_ret_7

; __device__ __forceinline__ unsigned xb_ld(unsigned* p)              { return __hip_atomic_load(p, __ATOMIC_RELAXED, __HIP_MEMORY_SCOPE_AGENT); }
; __device__ __forceinline__ unsigned xb_add(unsigned* p, unsigned v) { return __hip_atomic_fetch_add(p, v, __ATOMIC_RELAXED, __HIP_MEMORY_SCOPE_AGENT); }
; #define XB_SPIN(cond, bar) do { unsigned _sp = 0; while (cond) { __builtin_amdgcn_s_sleep(1); \
;     if ((++_sp & 255u) == 0u) { if (xb_ld(&(bar)[XB_TMO])) break; if (_sp > XB_SPIN_CAP) { atomicAdd(&(bar)[XB_TMO], 1u); break; } } } } while (0)
; #define SEAM(k) do { if (IN(k) && IN((k) + 1)) xcd_barrier(bar); } while (0)
; __device__ __forceinline__ void xcd_barrier(const XcdBarrier& b) {
;     asm volatile("s_waitcnt vmcnt(0)" ::: "memory");
;     __syncthreads();
;     if (threadIdx.x == 0) {
;         unsigned* bar = b.bar;
;         __builtin_amdgcn_s_waitcnt(0);
;         unsigned nloc = b.st[0], nx = b.st[1];
;         if (nloc == 0u) { xcd_barrier_complete(bar, b.x, nloc, nx); b.st[0] = nloc; b.st[1] = nx; }
;         const unsigned old = xb_add(&bar[XB_XSUB(b.x)], 1u);
;         const unsigned gen = old / nloc;
;         if (old + 1u == (gen + 1u) * nloc) {
;             __builtin_amdgcn_fence(__ATOMIC_RELEASE, "agent");
;             asm volatile("s_waitcnt vmcnt(0)" ::: "memory");
;             const unsigned og = xb_add(&bar[XB_TOP], 1u);
;             const unsigned tg = og / nx;
;             if (og + 1u == (tg + 1u) * nx) xb_add(&bar[XB_TOPGEN], 1u);
;             else XB_SPIN(xb_ld(&bar[XB_TOPGEN]) == tg, bar);
;             __builtin_amdgcn_fence(__ATOMIC_ACQUIRE, "agent");
;             xb_add(&bar[XB_XGEN(b.x)], 1u);
;             asm volatile("s_waitcnt vmcnt(0)" ::: "memory");
;         } else {
;             XB_SPIN(xb_ld(&bar[XB_XGEN(b.x)]) == gen, bar);
;             __builtin_amdgcn_fence(__ATOMIC_ACQUIRE, "agent");
;             asm volatile("s_waitcnt vmcnt(0)" ::: "memory");
;         }
;     }
;     __syncthreads();
; }
; __global__ void __launch_bounds__(NWAVES * 64, 2) mk_fwd(Args args) {
;     ...
;     SEAM(4);
;     if (IN(5)) {
;         pg8::Gemm g{(const bf16*)(ws + WS_MIX), (const bf16*)(ws + WS_WOUT), M, DM, DM, DM}; pg8::StaticOrder S; S.init(M, DM, G, bx);
;         pg8::EpiRes<1> E{nullptr, nullptr, HB, (float*)(ws + WS_SSQ1)};
;         STAGGER(1.5f); pg8::gemm_phase<pg8::EpiRes<1>, pg8::StaticOrder, true, true>(lds, g, S, E);
.LBB0_781:
	s_or_b64 exec, exec, s[4:5]
	s_cmp_lg_u32 s80, 0x100
	s_cbranch_scc1 .Lsh_skip_4
	s_cmp_lg_u32 s74, 0
	s_cbranch_scc1 .Lsh_skip_4
	s_cmp_lg_u32 s75, 12
	s_cbranch_scc1 .Lsh_skip_4
	v_readfirstlane_b32 s101, v0
	s_nop 3
	s_lshr_b32 s101, s101, 6
	s_cmp_eq_u32 s101, 0
	s_cbranch_scc1 .Lsh_skip_4
	v_writelane_b32 v255, s0, 20
	v_writelane_b32 v255, s1, 21
	v_writelane_b32 v255, s4, 22
	v_writelane_b32 v255, s5, 23
	v_writelane_b32 v255, s6, 24
	v_writelane_b32 v255, s7, 25
	v_writelane_b32 v255, s8, 26
	v_writelane_b32 v255, s9, 27
	v_writelane_b32 v255, s12, 28
	v_writelane_b32 v255, s16, 29
	v_writelane_b32 v255, s18, 30
	v_writelane_b32 v255, s19, 31
	v_writelane_b32 v255, s20, 32
	v_writelane_b32 v255, s21, 33
	v_writelane_b32 v255, s23, 34
	v_writelane_b32 v255, s24, 35
	v_writelane_b32 v255, s26, 36
	v_writelane_b32 v255, s34, 37
	v_readlane_b32 s70, v254, 0
	v_readlane_b32 s71, v254, 1
	v_and_b32_e32 v1, 63, v0
	s_mul_i32 s100, s2, 7
	s_nop 3
	s_sub_u32 s70, s70, 0xc0
	s_subb_u32 s71, s71, 0
	s_add_u32 s101, s101, s100
	s_sub_u32 s101, s101, 1
	s_mov_b32 s100, 224
	s_mov_b32 s0, 0x700
	v_writelane_b32 v255, s0, 2
	s_mov_b32 s0, 0x4400
	v_writelane_b32 v255, s0, 3
	s_mov_b32 s98, 4
	s_mov_b32 s99, 1
	s_mov_b64 s[4:5], -1
	s_branch .Lp4_conv_entry
.Lsh_ret_4:
	v_readlane_b32 s0, v255, 20
	v_readlane_b32 s1, v255, 21
	v_readlane_b32 s4, v255, 22
	v_readlane_b32 s5, v255, 23
	v_readlane_b32 s6, v255, 24
	v_readlane_b32 s7, v255, 25
	v_readlane_b32 s8, v255, 26
	v_readlane_b32 s9, v255, 27
	v_readlane_b32 s12, v255, 28
	v_readlane_b32 s16, v255, 29
	v_readlane_b32 s18, v255, 30
	v_readlane_b32 s19, v255, 31
	v_readlane_b32 s20, v255, 32
	v_readlane_b32 s21, v255, 33
	v_readlane_b32 s23, v255, 34
	v_readlane_b32 s24, v255, 35
	v_readlane_b32 s26, v255, 36
	v_readlane_b32 s34, v255, 37
	s_mov_b32 s98, 0
	s_mov_b32 s99, 0
	s_nop 3
.Lsh_skip_4:
	s_waitcnt lgkmcnt(0)
	s_barrier
.LBB0_782:
	s_cmp_lt_i32 s74, 6
	s_cselect_b64 s[4:5], -1, 0
	s_and_b64 s[6:7], s[4:5], s[0:1]
	s_andn2_b64 vcc, exec, s[6:7]
	s_cbranch_vccnz .LBB0_828
	s_bfe_u32 s3, s2, 0x30003
	v_cvt_f32_ubyte0_e32 v2, s3
	v_mul_f32_e32 v2, 0x3fc00000, v2
	v_mul_f32_e32 v2, 0, v2
	v_trunc_f32_e32 v2, v2
	s_memrealtime s[0:1]
	v_mul_f32_e32 v3, 0x2f800000, v2
	s_memrealtime s[4:5]
	v_floor_f32_e32 v3, v3
	v_fmamk_f32 v2, v3, 0xcf800000, v2
	v_cvt_u32_f32_e32 v2, v2
	v_cvt_u32_f32_e32 v3, v3
	s_waitcnt lgkmcnt(0)
	s_sub_u32 s4, s4, s0
	s_subb_u32 s5, s5, s1
	v_cmp_ge_u64_e32 vcc, s[4:5], v[2:3]
	s_cbranch_vccnz .LBB0_785

; __device__ __forceinline__ unsigned xb_ld(unsigned* p)              { return __hip_atomic_load(p, __ATOMIC_RELAXED, __HIP_MEMORY_SCOPE_AGENT); }
; __device__ __forceinline__ unsigned xb_add(unsigned* p, unsigned v) { return __hip_atomic_fetch_add(p, v, __ATOMIC_RELAXED, __HIP_MEMORY_SCOPE_AGENT); }
; #define XB_SPIN(cond, bar) do { unsigned _sp = 0; while (cond) { __builtin_amdgcn_s_sleep(1); \
;     if ((++_sp & 255u) == 0u) { if (xb_ld(&(bar)[XB_TMO])) break; if (_sp > XB_SPIN_CAP) { atomicAdd(&(bar)[XB_TMO], 1u); break; } } } } while (0)
; #define SEAM(k) do { if (IN(k) && IN((k) + 1)) xcd_barrier(bar); } while (0)
; __device__ __forceinline__ void xcd_barrier(const XcdBarrier& b) {
;     asm volatile("s_waitcnt vmcnt(0)" ::: "memory");
;     __syncthreads();
;     if (threadIdx.x == 0) {
;         unsigned* bar = b.bar;
;         __builtin_amdgcn_s_waitcnt(0);
;         unsigned nloc = b.st[0], nx = b.st[1];
;         if (nloc == 0u) { xcd_barrier_complete(bar, b.x, nloc, nx); b.st[0] = nloc; b.st[1] = nx; }
;         const unsigned old = xb_add(&bar[XB_XSUB(b.x)], 1u);
;         const unsigned gen = old / nloc;
;         if (old + 1u == (gen + 1u) * nloc) {
;             __builtin_amdgcn_fence(__ATOMIC_RELEASE, "agent");
;             asm volatile("s_waitcnt vmcnt(0)" ::: "memory");
;             const unsigned og = xb_add(&bar[XB_TOP], 1u);
;             const unsigned tg = og / nx;
;             if (og + 1u == (tg + 1u) * nx) xb_add(&bar[XB_TOPGEN], 1u);
;             else XB_SPIN(xb_ld(&bar[XB_TOPGEN]) == tg, bar);
;             __builtin_amdgcn_fence(__ATOMIC_ACQUIRE, "agent");
;             xb_add(&bar[XB_XGEN(b.x)], 1u);
;             asm volatile("s_waitcnt vmcnt(0)" ::: "memory");
;         } else {
;             XB_SPIN(xb_ld(&bar[XB_XGEN(b.x)]) == gen, bar);
;             __builtin_amdgcn_fence(__ATOMIC_ACQUIRE, "agent");
;             asm volatile("s_waitcnt vmcnt(0)" ::: "memory");
;         }
;     }
;     __syncthreads();
; }
; __global__ void __launch_bounds__(NWAVES * 64, 2) mk_fwd(Args args) {
;     ...
;     SEAM(5);
;     if (IN(6)) {
.LBB0_881:
	s_or_b64 exec, exec, s[4:5]
	s_cmp_lg_u32 s80, 0x100
	s_cbranch_scc1 .Lsh_skip_5
	s_cmp_lg_u32 s74, 0
	s_cbranch_scc1 .Lsh_skip_5
	s_cmp_lg_u32 s75, 12
	s_cbranch_scc1 .Lsh_skip_5
	v_readfirstlane_b32 s101, v0
	s_nop 3
	s_lshr_b32 s101, s101, 6
	s_cmp_eq_u32 s101, 0
	s_cbranch_scc1 .Lsh_skip_5
	v_writelane_b32 v255, s0, 20
	v_writelane_b32 v255, s1, 21
	v_writelane_b32 v255, s4, 22
	v_writelane_b32 v255, s5, 23
	v_writelane_b32 v255, s6, 24
	v_writelane_b32 v255, s7, 25
	v_writelane_b32 v255, s8, 26
	v_writelane_b32 v255, s9, 27
	v_writelane_b32 v255, s12, 28
	v_writelane_b32 v255, s16, 29
	v_writelane_b32 v255, s18, 30
	v_writelane_b32 v255, s19, 31
	v_writelane_b32 v255, s20, 32
	v_writelane_b32 v255, s21, 33
	v_writelane_b32 v255, s23, 34
	v_writelane_b32 v255, s24, 35
	v_writelane_b32 v255, s26, 36
	v_writelane_b32 v255, s34, 37
	v_readlane_b32 s70, v254, 0
	v_readlane_b32 s71, v254, 1
	v_and_b32_e32 v1, 63, v0
	s_mul_i32 s100, s2, 7
	s_nop 3
	s_sub_u32 s70, s70, 0xc0
	s_subb_u32 s71, s71, 0
	s_add_u32 s101, s101, s100
	s_sub_u32 s101, s101, 1
	s_mov_b32 s100, 224
	s_mov_b32 s0, 0x700
	v_writelane_b32 v255, s0, 2
	s_mov_b32 s0, 0x4b00
	v_writelane_b32 v255, s0, 3
	s_mov_b32 s98, 5
	s_mov_b32 s99, 1
	s_mov_b64 s[4:5], -1
	s_branch .Lp4_conv_entry

; template <class Epi, class Sched, bool ALIGN_EPI = false, bool SP2 = false, bool HALFM = false>
; __device__ __forceinline__ void gemm_phase(PG8_LAS unsigned char* lds, const Gemm g, const Sched& S, const Epi& E) {
;     const int tid = threadIdx.x, wid = __builtin_amdgcn_readfirstlane(tid >> 6), lane = tid & 63, wr = wid >> 2, wc = wid & 3, fr = lane & 15, fq = lane >> 4;
;     const int K = g.K, nt = K / BK;
;     unsigned voffA[2], voffB[2];
; #pragma unroll
;     for (int i = 0; i < 2; ++i) { voffA[i] = (unsigned)(tid * 16 + i * 8192); voffB[i] = voffA[i]; }
;     const size_t kstep = 32768;
;     const size_t hstep = 16384, hstepA = 16384;
;     const size_t tstep = (size_t)K * 512, tstepA = (size_t)g.lda * 512;
;     const unsigned ldsw = (unsigned)wid * 1024u;
;     const int aoff = lds_byte(wr * 64 + fr, fq * 8), boff = lds_byte(wc * 32 + fr, fq * 8);
; __global__ void __launch_bounds__(NWAVES * 64, 2) mk_fwd(Args args) {
;     ...
;     if (IN(6)) {
;         { pg8::Gemm g{HB, (const bf16*)(ws + WS_WQKV), M, CW, DM, DM}; pg8::StaticOrder S; S.init(M, CW, G, bx);
;           pg8::EpiScaleF32 E{(float*)(ws + WS_CQ), CW, (const float*)(ws + WS_SSQ1)};
;           pg8::gemm_phase<pg8::EpiScaleF32, pg8::StaticOrder, true, true>(lds, g, S, E); }
.Lsh_skip_5:
	s_waitcnt lgkmcnt(0)
	s_barrier
.LBB0_882:
	s_cmp_lt_i32 s74, 7
	s_cselect_b64 s[4:5], -1, 0
	s_and_b64 s[8:9], s[4:5], s[0:1]
	s_andn2_b64 vcc, exec, s[8:9]
	v_lshrrev_b32_e32 v204, 1, v0
	s_cbranch_vccnz .LBB0_925
	s_waitcnt vmcnt(0)
	v_and_b32_e32 v143, 24, v204
	v_lshlrev_b32_e32 v2, 6, v0
	s_waitcnt lgkmcnt(0)
	v_lshlrev_b32_e32 v3, 2, v0
	v_lshlrev_b32_e32 v130, 4, v0
	v_lshlrev_b32_e32 v145, 1, v143
	v_and_b32_e32 v2, 0x3c0, v2
	v_and_b32_e32 v3, 32, v3
	s_ashr_i32 s3, s80, 31
	v_readfirstlane_b32 s20, v0
	v_or_b32_e32 v142, 0x2000, v130
	v_and_b32_e32 v144, 15, v0
	s_cmpk_gt_i32 s2, 0x7f
	v_bitop3_b32 v146, v145, v3, v2 bitop3:0x36
	s_cbranch_scc1 .LBB0_908
	s_ashr_i32 s33, s2, 31
	s_lshr_b32 s0, s33, 29
	s_add_i32 s4, s2, s0
	s_and_b32 s0, s4, -8
	s_sub_i32 s6, s2, s0
	s_cmp_gt_i32 s6, -1
	s_cbranch_scc0 .LBB0_886
	s_lshl_b32 s5, s6, 4
	s_cbranch_execz .LBB0_887
	s_branch .LBB0_888

; __device__ __forceinline__ unsigned xb_ld(unsigned* p)              { return __hip_atomic_load(p, __ATOMIC_RELAXED, __HIP_MEMORY_SCOPE_AGENT); }
; __device__ __forceinline__ unsigned xb_add(unsigned* p, unsigned v) { return __hip_atomic_fetch_add(p, v, __ATOMIC_RELAXED, __HIP_MEMORY_SCOPE_AGENT); }
; #define XB_SPIN(cond, bar) do { unsigned _sp = 0; while (cond) { __builtin_amdgcn_s_sleep(1); \
;     if ((++_sp & 255u) == 0u) { if (xb_ld(&(bar)[XB_TMO])) break; if (_sp > XB_SPIN_CAP) { atomicAdd(&(bar)[XB_TMO], 1u); break; } } } } while (0)
; #define SEAM(k) do { if (IN(k) && IN((k) + 1)) xcd_barrier(bar); } while (0)
; __device__ __forceinline__ void xcd_barrier(const XcdBarrier& b) {
;     asm volatile("s_waitcnt vmcnt(0)" ::: "memory");
;     __syncthreads();
;     if (threadIdx.x == 0) {
;         unsigned* bar = b.bar;
;         __builtin_amdgcn_s_waitcnt(0);
;         unsigned nloc = b.st[0], nx = b.st[1];
;         if (nloc == 0u) { xcd_barrier_complete(bar, b.x, nloc, nx); b.st[0] = nloc; b.st[1] = nx; }
;         const unsigned old = xb_add(&bar[XB_XSUB(b.x)], 1u);
;         const unsigned gen = old / nloc;
;         if (old + 1u == (gen + 1u) * nloc) {
;             __builtin_amdgcn_fence(__ATOMIC_RELEASE, "agent");
;             asm volatile("s_waitcnt vmcnt(0)" ::: "memory");
;             const unsigned og = xb_add(&bar[XB_TOP], 1u);
;             const unsigned tg = og / nx;
;             if (og + 1u == (tg + 1u) * nx) xb_add(&bar[XB_TOPGEN], 1u);
;             else XB_SPIN(xb_ld(&bar[XB_TOPGEN]) == tg, bar);
;             __builtin_amdgcn_fence(__ATOMIC_ACQUIRE, "agent");
;             xb_add(&bar[XB_XGEN(b.x)], 1u);
;             asm volatile("s_waitcnt vmcnt(0)" ::: "memory");
;         } else {
;             XB_SPIN(xb_ld(&bar[XB_XGEN(b.x)]) == gen, bar);
;             __builtin_amdgcn_fence(__ATOMIC_ACQUIRE, "agent");
;             asm volatile("s_waitcnt vmcnt(0)" ::: "memory");
;         }
;     }
;     __syncthreads();
; }
; __global__ void __launch_bounds__(NWAVES * 64, 2) mk_fwd(Args args) {
;     ...
;     SEAM(6);
;     if (IN(7)) { for (int u = bx; u < 256; u += G) cross_unit(lds, (const float*)(ws + WS_CQ), (const float*)(ws + WS_CKV), P.cq_norm, P.ck_norm, (bf16*)(ws + WS_CO), u, tid); __syncthreads(); }
.LBB0_978:
	s_or_b64 exec, exec, s[4:5]
	s_cmp_lg_u32 s80, 0x100
	s_cbranch_scc1 .Lsh_skip_6
	s_cmp_lg_u32 s74, 0
	s_cbranch_scc1 .Lsh_skip_6
	s_cmp_lg_u32 s75, 12
	s_cbranch_scc1 .Lsh_skip_6
	v_readfirstlane_b32 s101, v0
	s_nop 3
	s_lshr_b32 s101, s101, 6
	s_cmp_eq_u32 s101, 0
	s_cbranch_scc1 .Lsh_skip_6
	v_writelane_b32 v255, s0, 20
	v_writelane_b32 v255, s1, 21
	v_writelane_b32 v255, s4, 22
	v_writelane_b32 v255, s5, 23
	v_writelane_b32 v255, s6, 24
	v_writelane_b32 v255, s7, 25
	v_writelane_b32 v255, s8, 26
	v_writelane_b32 v255, s9, 27
	v_writelane_b32 v255, s12, 28
	v_writelane_b32 v255, s16, 29
	v_writelane_b32 v255, s18, 30
	v_writelane_b32 v255, s19, 31
	v_writelane_b32 v255, s20, 32
	v_writelane_b32 v255, s21, 33
	v_writelane_b32 v255, s23, 34
	v_writelane_b32 v255, s24, 35
	v_writelane_b32 v255, s26, 36
	v_writelane_b32 v255, s34, 37
	v_readlane_b32 s70, v254, 0
	v_readlane_b32 s71, v254, 1
	v_and_b32_e32 v1, 63, v0
	s_mul_i32 s100, s2, 7
	s_nop 3
	s_sub_u32 s70, s70, 0xc0
	s_subb_u32 s71, s71, 0
	s_add_u32 s101, s101, s100
	s_sub_u32 s101, s101, 1
	s_mov_b32 s100, 224
	s_mov_b32 s0, 0x700
	v_writelane_b32 v255, s0, 2
	s_mov_b32 s0, 0x5200
	v_writelane_b32 v255, s0, 3
	s_mov_b32 s98, 6
	s_mov_b32 s99, 1
	s_mov_b64 s[4:5], -1
	s_branch .Lp4_conv_entry

; #define LAS __attribute__((address_space(3)))
; #define GAS __attribute__((address_space(1)))
; #define LAS __attribute__((address_space(3)))
; DI void cross_unit(LAS unsigned char* lds, const float* CQ, const float* CKV, const float* gq, const float* gk, bf16* CO, int unit, int tid) {
;     const int lane = tid & 63, w = __builtin_amdgcn_readfirstlane(tid >> 6), r = lane & 31, h = lane >> 5;
;     const int qb = unit & 31, ch = (unit >> 5) & 3, b = unit >> 7;
;     LAS unsigned char* KT = lds + L_KT; LAS unsigned char* VT = lds + L_VT; LAS float* RKc = (LAS float*)(lds + L_RK);
;     const size_t qrow = (size_t)b * SEQ + 256 * qb + 32 * w + r;
;     __syncthreads();
;     {
;         const int key = tid >> 1, half = tid & 1; const float* src = CKV + (size_t)(b * NMEM + key) * (2 * CW) + 128 * ch + 64 * half; float s = 0.f;
; #pragma unroll
;         for (int j = 0; j < 16; ++j) { const f32x4 v = *(const GAS f32x4*)(src + 4 * j); s += (v.x * v.x + v.y * v.y) + (v.z * v.z + v.w * v.w); }
;         s += __shfl_xor(s, 1);
;         if (half == 0) RKc[key] = rsqrtf(s * (1.0f / 128.0f) + EPSN);
;     }
;     bf16x8 qf[8];
;     {
;         const float* qp = CQ + qrow * CW + 128 * ch; f32x4 qv[8][2]; float s = 0.f;
; #pragma unroll
;         for (int ks = 0; ks < 8; ++ks) { qv[ks][0] = *(const GAS f32x4*)(qp + 16 * ks + 8 * h); qv[ks][1] = *(const GAS f32x4*)(qp + 16 * ks + 8 * h + 4);
;             s += (qv[ks][0].x * qv[ks][0].x + qv[ks][0].y * qv[ks][0].y) + (qv[ks][0].z * qv[ks][0].z + qv[ks][0].w * qv[ks][0].w) + (qv[ks][1].x * qv[ks][1].x + qv[ks][1].y * qv[ks][1].y) + (qv[ks][1].z * qv[ks][1].z + qv[ks][1].w * qv[ks][1].w); }
;         s += __shfl_xor(s, 32);
;         const float rs = rsqrtf(s * (1.0f / 128.0f) + EPSN) * 0.08838834764831845f;
; #pragma unroll
;         for (int ks = 0; ks < 8; ++ks) { const f32x4 g0 = *(const f32x4*)(gq + 16 * ks + 8 * h), g1 = *(const f32x4*)(gq + 16 * ks + 8 * h + 4); const f32x4 a0 = qv[ks][0] * g0 * rs, a1 = qv[ks][1] * g1 * rs;
;             qf[ks] = pack8(a0[0], a0[1], a0[2], a0[3], a1[0], a1[1], a1[2], a1[3]); }
;     }
;     __syncthreads();
; __global__ void __launch_bounds__(NWAVES * 64, 2) mk_fwd(Args args) {
;     ...
;     if (IN(7)) { for (int u = bx; u < 256; u += G) cross_unit(lds, (const float*)(ws + WS_CQ), (const float*)(ws + WS_CKV), P.cq_norm, P.ck_norm, (bf16*)(ws + WS_CO), u, tid); __syncthreads(); }
.Lsh_skip_6:
	s_waitcnt lgkmcnt(0)
	s_barrier
.LBB0_979:
	s_cmp_lt_i32 s74, 8
	s_cselect_b64 s[4:5], -1, 0
	s_and_b64 s[8:9], s[4:5], s[0:1]
	s_andn2_b64 vcc, exec, s[8:9]
	s_cbranch_vccnz .LBB0_1002
	s_cmpk_gt_i32 s2, 0xff
	s_cbranch_scc1 .LBB0_1001
	v_mbcnt_lo_u32_b32 v5, -1, 0
	s_add_u32 s10, s84, 0x1a00000
	v_mbcnt_hi_u32_b32 v5, -1, v5
	s_addc_u32 s11, s85, 0
	v_and_b32_e32 v7, 64, v5
	s_add_u32 s12, s84, 0x3a00000
	s_waitcnt lgkmcnt(0)
	v_and_b32_e32 v3, 1, v0
	v_xor_b32_e32 v6, 1, v5
	v_add_u32_e32 v7, 64, v7
	s_addc_u32 s13, s85, 0
	v_lshlrev_b32_e32 v2, 6, v3
	v_cmp_lt_i32_e32 vcc, v6, v7
	v_cmp_eq_u32_e64 s[0:1], 0, v3
	v_xor_b32_e32 v3, 32, v5
	s_add_u32 s14, s84, 0x3c00000
	v_cndmask_b32_e32 v6, v5, v6, vcc
	v_cmp_lt_i32_e32 vcc, v3, v7
	v_readlane_b32 s36, v254, 18
	s_addc_u32 s15, s85, 0
	v_bfe_u32 v4, v0, 5, 1
	s_add_i32 s3, 0, 0x14000
	v_cndmask_b32_e32 v3, v5, v3, vcc
	v_readlane_b32 s46, v254, 28
	v_readlane_b32 s47, v254, 29
	s_waitcnt vmcnt(0)
	v_and_b32_e32 v141, 31, v0
	v_mov_b32_e32 v139, 0
	v_lshl_add_u32 v159, v204, 2, s3
	v_lshlrev_b32_e32 v160, 2, v3
	v_lshlrev_b32_e32 v138, 5, v4
	s_mov_b64 s[18:19], s[46:47]
	v_and_b32_e32 v3, 15, v0
	v_lshlrev_b32_e32 v5, 4, v4
	v_lshrrev_b32_e32 v162, 4, v0
	s_movk_i32 s3, 0x110
	v_lshl_add_u64 v[142:143], s[18:19], 0, v[138:139]
	v_lshlrev_b32_e32 v138, 5, v3
	v_lshlrev_b32_e32 v3, 4, v3
	v_mul_u32_u24_e32 v7, 0x110, v162
	v_mad_u32_u24 v165, v141, s3, v5
	v_mul_u32_u24_e32 v5, 0x140, v162
	v_lshlrev_b32_e32 v158, 2, v6
	v_bfe_u32 v6, v0, 2, 2
	v_add3_u32 v163, v7, v3, 0
	v_add3_u32 v3, v5, v3, 0
	v_add_u32_e32 v169, 0xa000, v3
	v_mul_u32_u24_e32 v3, 0x140, v6
	s_movk_i32 s3, 0x500
	v_lshlrev_b32_e32 v140, 3, v4
	v_readlane_b32 s48, v254, 30
	v_readlane_b32 s49, v254, 31
	v_mad_u32_u24 v3, v4, s3, v3
	v_lshlrev_b32_e32 v4, 1, v0
	v_and_b32_e32 v5, 3, v0
	s_mov_b64 s[20:21], s[48:49]
	v_lshl_add_u32 v7, v162, 2, 0
	v_and_b32_e32 v4, 32, v4
	v_lshlrev_b32_e32 v5, 3, v5
	s_mov_b32 s17, 0
	v_lshl_add_u64 v[144:145], s[12:13], 0, v[138:139]
	v_lshl_add_u64 v[146:147], s[20:21], 0, v[138:139]
	v_or_b32_e32 v161, 0xfffffe00, v0
	v_add_u32_e32 v164, 0x14000, v7
	v_add_u32_e32 v166, 0, v165
	v_add_u32_e32 v167, 0x14200, v7
	v_or_b32_e32 v168, 0x80, v162
	v_or3_b32 v170, v3, v4, v5
	v_lshlrev_b32_e32 v148, 2, v2
	v_mov_b32_e32 v149, v139
	v_mov_b32_e32 v171, 0x358637bd
	s_mov_b32 s3, 0x800000
	v_lshlrev_b32_e32 v138, 2, v140
	s_movk_i32 s18, 0x5ff
	s_movk_i32 s19, 0x3c0
	s_mov_b32 s20, s2
	v_readlane_b32 s37, v254, 19
	v_readlane_b32 s38, v254, 20
	v_readlane_b32 s39, v254, 21
	v_readlane_b32 s40, v254, 22
	v_readlane_b32 s41, v254, 23
	v_readlane_b32 s42, v254, 24
	v_readlane_b32 s43, v254, 25
	v_readlane_b32 s44, v254, 26
	v_readlane_b32 s45, v254, 27
	v_readlane_b32 s50, v254, 32
	v_readlane_b32 s51, v254, 33

; __device__ __forceinline__ unsigned xb_ld(unsigned* p)              { return __hip_atomic_load(p, __ATOMIC_RELAXED, __HIP_MEMORY_SCOPE_AGENT); }
; __device__ __forceinline__ unsigned xb_add(unsigned* p, unsigned v) { return __hip_atomic_fetch_add(p, v, __ATOMIC_RELAXED, __HIP_MEMORY_SCOPE_AGENT); }
; #define XB_SPIN(cond, bar) do { unsigned _sp = 0; while (cond) { __builtin_amdgcn_s_sleep(1); \
;     if ((++_sp & 255u) == 0u) { if (xb_ld(&(bar)[XB_TMO])) break; if (_sp > XB_SPIN_CAP) { atomicAdd(&(bar)[XB_TMO], 1u); break; } } } } while (0)
; #define SEAM(k) do { if (IN(k) && IN((k) + 1)) xcd_barrier(bar); } while (0)
; __device__ __forceinline__ void xcd_barrier(const XcdBarrier& b) {
;     asm volatile("s_waitcnt vmcnt(0)" ::: "memory");
;     __syncthreads();
;     if (threadIdx.x == 0) {
;         unsigned* bar = b.bar;
;         __builtin_amdgcn_s_waitcnt(0);
;         unsigned nloc = b.st[0], nx = b.st[1];
;         if (nloc == 0u) { xcd_barrier_complete(bar, b.x, nloc, nx); b.st[0] = nloc; b.st[1] = nx; }
;         const unsigned old = xb_add(&bar[XB_XSUB(b.x)], 1u);
;         const unsigned gen = old / nloc;
;         if (old + 1u == (gen + 1u) * nloc) {
;             __builtin_amdgcn_fence(__ATOMIC_RELEASE, "agent");
;             asm volatile("s_waitcnt vmcnt(0)" ::: "memory");
;             const unsigned og = xb_add(&bar[XB_TOP], 1u);
;             const unsigned tg = og / nx;
;             if (og + 1u == (tg + 1u) * nx) xb_add(&bar[XB_TOPGEN], 1u);
;             else XB_SPIN(xb_ld(&bar[XB_TOPGEN]) == tg, bar);
;             __builtin_amdgcn_fence(__ATOMIC_ACQUIRE, "agent");
;             xb_add(&bar[XB_XGEN(b.x)], 1u);
;             asm volatile("s_waitcnt vmcnt(0)" ::: "memory");
;         } else {
;             XB_SPIN(xb_ld(&bar[XB_XGEN(b.x)]) == gen, bar);
;             __builtin_amdgcn_fence(__ATOMIC_ACQUIRE, "agent");
;             asm volatile("s_waitcnt vmcnt(0)" ::: "memory");
;         }
;     }
;     __syncthreads();
; }
; __global__ void __launch_bounds__(NWAVES * 64, 2) mk_fwd(Args args) {
;     ...
;     SEAM(7);
;     if (IN(8)) {
.LBB0_1055:
	s_or_b64 exec, exec, s[4:5]
	s_cmp_lg_u32 s80, 0x100
	s_cbranch_scc1 .Lsh_skip_7
	s_cmp_lg_u32 s74, 0
	s_cbranch_scc1 .Lsh_skip_7
	s_cmp_lg_u32 s75, 12
	s_cbranch_scc1 .Lsh_skip_7
	v_readfirstlane_b32 s101, v0
	s_nop 3
	s_lshr_b32 s101, s101, 6
	s_cmp_eq_u32 s101, 0
	s_cbranch_scc1 .Lsh_skip_7
	v_writelane_b32 v255, s0, 20
	v_writelane_b32 v255, s1, 21
	v_writelane_b32 v255, s4, 22
	v_writelane_b32 v255, s5, 23
	v_writelane_b32 v255, s6, 24
	v_writelane_b32 v255, s7, 25
	v_writelane_b32 v255, s8, 26
	v_writelane_b32 v255, s9, 27
	v_writelane_b32 v255, s12, 28
	v_writelane_b32 v255, s16, 29
	v_writelane_b32 v255, s18, 30
	v_writelane_b32 v255, s19, 31
	v_writelane_b32 v255, s20, 32
	v_writelane_b32 v255, s21, 33
	v_writelane_b32 v255, s23, 34
	v_writelane_b32 v255, s24, 35
	v_writelane_b32 v255, s26, 36
	v_writelane_b32 v255, s34, 37
	v_readlane_b32 s70, v254, 0
	v_readlane_b32 s71, v254, 1
	v_and_b32_e32 v1, 63, v0
	s_mul_i32 s100, s2, 7
	s_nop 3
	s_sub_u32 s70, s70, 0xc0
	s_subb_u32 s71, s71, 0
	s_add_u32 s101, s101, s100
	s_sub_u32 s101, s101, 1
	s_mov_b32 s100, 224
	s_mov_b32 s0, 0x700
	v_writelane_b32 v255, s0, 2
	s_mov_b32 s0, 0x5900
	v_writelane_b32 v255, s0, 3
	s_mov_b32 s98, 7
	s_mov_b32 s99, 1
	s_mov_b64 s[4:5], -1
	s_branch .Lp4_conv_entry

; #define SEAM(k) do { if (IN(k) && IN((k) + 1)) xcd_barrier(bar); } while (0)
; #define STAGGER(step_us) do { const unsigned long long _t0 = __builtin_amdgcn_s_memrealtime(), _d = (unsigned long long)(((bx >> 3) & 7) * (step_us) * (100.0f * STAGGER_SCALE)); \
;         while (__builtin_amdgcn_s_memrealtime() - _t0 < _d) __builtin_amdgcn_s_sleep(8); } while (0)
; __global__ void __launch_bounds__(NWAVES * 64, 2) mk_fwd(Args args) {
;     ...
;     SEAM(7);
;     if (IN(8)) {
;         pg8::Gemm g{(const bf16*)(ws + WS_CO), (const bf16*)(ws + WS_WO), M, DM, CW, CW}; pg8::StaticOrder S; S.init(M, DM, G, bx);
;         pg8::EpiRes<1> E{nullptr, nullptr, HB, (float*)(ws + WS_SSQ2)};
;         STAGGER(1.5f); pg8::gemm_phase<pg8::EpiRes<1>, pg8::StaticOrder, true, true>(lds, g, S, E);
.Lsh_skip_7:
	s_waitcnt lgkmcnt(0)
	s_barrier
.LBB0_1056:
	s_cmp_lt_i32 s74, 9
	s_cselect_b64 s[4:5], -1, 0
	s_and_b64 s[6:7], s[4:5], s[0:1]
	s_andn2_b64 vcc, exec, s[6:7]
	s_cbranch_vccnz .LBB0_1102
	s_bfe_u32 s3, s2, 0x30003
	v_cvt_f32_ubyte0_e32 v2, s3
	v_mul_f32_e32 v2, 0x3fc00000, v2
	v_mul_f32_e32 v2, 0, v2
	v_trunc_f32_e32 v2, v2
	s_memrealtime s[0:1]
	s_waitcnt lgkmcnt(0)
	v_mul_f32_e32 v3, 0x2f800000, v2
	s_memrealtime s[4:5]
	v_floor_f32_e32 v3, v3
	v_fmamk_f32 v2, v3, 0xcf800000, v2
	v_cvt_u32_f32_e32 v2, v2
	v_cvt_u32_f32_e32 v3, v3
	s_waitcnt lgkmcnt(0)
	s_sub_u32 s4, s4, s0
	s_subb_u32 s5, s5, s1
	v_cmp_ge_u64_e32 vcc, s[4:5], v[2:3]
	s_cbranch_vccnz .LBB0_1059
